# speedup vs baseline: 1.0140x; 1.0035x over previous
_Z11lstm_kernelPKiPKhPKfS4_S4_Pf:
	s_load_dwordx4 s[12:15], s[0:1], 0x0
	v_readfirstlane_b32 s19, v0
	v_or_b32_e32 v3, 0x400, v0
	s_movk_i32 s4, 0x500
	s_lshr_b32 s7, s19, 6
	s_lshl_b32 s18, s2, 6
	s_mulk_i32 s2, 0x1400
	v_mov_b32_e32 v2, 0x4ff
	v_cmp_gt_u32_e32 vcc, s4, v3
	s_mul_hi_i32 s3, s18, 0x50
	s_waitcnt lgkmcnt(0)
	s_add_u32 s2, s12, s2
	v_cndmask_b32_e32 v2, v2, v3, vcc
	s_addc_u32 s3, s13, s3
	v_lshlrev_b32_e32 v1, 2, v0
	v_lshlrev_b32_e32 v4, 2, v2
	s_movk_i32 s4, 0x184
	v_or_b32_e32 v28, 0x200, v0
	global_load_dword v29, v1, s[2:3]
	global_load_dword v30, v1, s[2:3] offset:2048
	global_load_dword v2, v4, s[2:3]
	v_mov_b32_e32 v4, 0x383
	v_cmp_gt_u32_e32 vcc, s4, v0
	s_add_u32 s2, s14, 0x34000
	s_addc_u32 s3, s15, 0
	v_cndmask_b32_e32 v4, v4, v28, vcc
	v_lshlrev_b32_e32 v31, 4, v0
	v_lshlrev_b32_e32 v4, 4, v4
	global_load_dwordx4 v[6:9], v31, s[2:3]
	global_load_dwordx4 v[10:13], v4, s[2:3]
	v_and_b32_e32 v4, 0x7f, v0
	v_lshlrev_b32_e32 v18, 4, v4
	v_mov_b32_e32 v19, 0
	v_lshl_add_u64 v[4:5], s[14:15], 0, v[18:19]
	s_mov_b32 s2, 0x37000
	v_add_co_u32_e64 v4, s[2:3], s2, v4
	s_nop 1
	v_addc_co_u32_e64 v5, s[2:3], 0, v5, s[2:3]
	global_load_dwordx4 v[14:17], v[4:5], off offset:2112
	s_movk_i32 s22, 0x410
	s_movk_i32 s2, 0x4ff
	v_and_b32_e32 v4, 63, v0
	v_cmp_lt_u32_e64 s[2:3], s2, v3
	s_mul_i32 s5, s7, 0x6000
	s_mul_hi_u32 s4, s7, 0x6000
	s_add_u32 s8, s14, s5
	s_addc_u32 s9, s15, s4
	v_lshlrev_b32_e32 v210, 4, v4
	v_mov_b32_e32 v211, v19
	v_lshl_add_u64 v[20:21], s[8:9], 0, v[210:211]
	s_movk_i32 s4, 0x2000
	v_add_co_u32_e64 v22, s[4:5], s4, v20
	s_nop 1
	v_addc_co_u32_e64 v23, s[4:5], 0, v21, s[4:5]
	s_movk_i32 s4, 0x3000
	s_nop 0
	v_add_co_u32_e64 v24, s[4:5], s4, v20
	global_load_dwordx4 v[90:93], v[22:23], off offset:1024
	global_load_dwordx4 v[86:89], v[22:23], off offset:2048
	v_addc_co_u32_e64 v25, s[4:5], 0, v21, s[4:5]
	s_movk_i32 s4, 0x5000
	s_nop 0
	v_add_co_u32_e64 v26, s[4:5], s4, v20
	s_nop 1
	v_addc_co_u32_e64 v27, s[4:5], 0, v21, s[4:5]
	global_load_dwordx4 v[82:85], v[22:23], off offset:3072
	global_load_dwordx4 v[46:49], v[26:27], off
	global_load_dwordx4 v[42:45], v[26:27], off offset:1024
	global_load_dwordx4 v[38:41], v[26:27], off offset:2048
	global_load_dwordx4 v[94:97], v[24:25], off offset:-4096
	global_load_dwordx4 v[34:37], v[26:27], off offset:3072
	s_movk_i32 s4, 0x1000
	v_add_co_u32_e64 v22, s[4:5], s4, v20
	global_load_dwordx4 v[126:129], v210, s[8:9]
	global_load_dwordx4 v[122:125], v210, s[8:9] offset:1024
	global_load_dwordx4 v[118:121], v210, s[8:9] offset:2048
	global_load_dwordx4 v[114:117], v210, s[8:9] offset:3072
	v_addc_co_u32_e64 v23, s[4:5], 0, v21, s[4:5]
	global_load_dwordx4 v[110:113], v[22:23], off
	global_load_dwordx4 v[106:109], v[22:23], off offset:1024
	global_load_dwordx4 v[102:105], v[22:23], off offset:2048
	global_load_dwordx4 v[98:101], v[22:23], off offset:3072
	global_load_dwordx4 v[78:81], v[24:25], off
	global_load_dwordx4 v[74:77], v[24:25], off offset:1024
	global_load_dwordx4 v[70:73], v[24:25], off offset:2048
	global_load_dwordx4 v[66:69], v[24:25], off offset:3072
	s_movk_i32 s4, 0x4000
	v_add_co_u32_e64 v20, s[4:5], s4, v20
	v_mov_b32_e32 v5, 0x4000
	s_nop 0
	v_addc_co_u32_e64 v21, s[4:5], 0, v21, s[4:5]
	global_load_dwordx4 v[62:65], v[20:21], off
	global_load_dwordx4 v[58:61], v[20:21], off offset:1024
	global_load_dwordx4 v[54:57], v[20:21], off offset:2048
	global_load_dwordx4 v[50:53], v[20:21], off offset:3072
	s_waitcnt vmcnt(26)
	ds_write_b128 v31, v[6:9] offset:16384
	v_lshl_or_b32 v5, v28, 4, v5
	v_add_u32_e32 v6, 0x9840, v31
	v_cndmask_b32_e32 v5, v6, v5, vcc
	s_waitcnt vmcnt(25)
	ds_write_b128 v5, v[10:13]
	s_waitcnt vmcnt(24)
	ds_write_b128 v18, v[14:17] offset:36928
	v_mul_u32_u24_e32 v5, 0xccd, v0
	v_lshrrev_b32_e32 v5, 16, v5
	s_mov_b32 s5, 0xffffec
	v_mul_u32_u24_e32 v6, 0xccd, v28
	s_movk_i32 s4, 0x90
	v_mad_u32_u24 v8, v5, s5, v0
	v_lshlrev_b32_e32 v5, 2, v5
	v_lshrrev_b32_e32 v6, 16, v6
	v_mul_lo_u32 v7, v29, s4
	v_lshl_or_b32 v5, v8, 8, v5
	ds_write_b32 v5, v7 offset:30784
	v_mul_lo_u32 v196, v29, s22
	v_add_u32_e32 v197, 0x24e80, v5
	ds_write_b32 v197, v196
	v_mad_u32_u24 v7, v6, s5, v28
	v_lshlrev_b32_e32 v6, 2, v6
	v_mul_lo_u32 v5, v30, s4
	v_lshl_or_b32 v6, v7, 8, v6
	ds_write_b32 v6, v5 offset:30784
	v_mul_lo_u32 v198, v30, s22
	v_add_u32_e32 v199, 0x24e80, v6
	ds_write_b32 v199, v198
	s_and_saveexec_b64 s[4:5], s[2:3]
	s_xor_b64 s[2:3], exec, s[4:5]
	v_mov_b32_e32 v3, 0x9840
	v_lshl_add_u32 v5, v0, 2, v3
	s_andn2_saveexec_b64 s[2:3], s[2:3]
	v_mul_u32_u24_e32 v5, 0xccd, v3
	s_mov_b32 s4, 0xffffec
	v_mul_u32_u24_sdwa v6, v5, s4 dst_sel:DWORD dst_unused:UNUSED_PAD src0_sel:WORD_1 src1_sel:DWORD
	v_add_lshl_u32 v3, v6, v3, 8
	v_mov_b32_e32 v6, 2
	v_lshlrev_b32_sdwa v5, v6, v5 dst_sel:DWORD dst_unused:UNUSED_PAD src0_sel:DWORD src1_sel:WORD_1
	s_movk_i32 s4, 0x7840
	v_add3_u32 v5, v5, v3, s4
	s_or_b64 exec, exec, s[2:3]
	v_lshrrev_b32_e32 v3, 5, v4
	s_movk_i32 s2, 0x90
	s_lshl_b32 s6, s7, 10
	s_mulk_i32 s7, 0xfd00
	v_and_b32_e32 v182, 31, v0
	v_mul_lo_u32 v200, v2, s22
	v_mul_lo_u32 v2, v2, s2
	s_add_i32 s7, s6, s7
	v_lshlrev_b32_e32 v229, 6, v3
	ds_write_b32 v5, v2
	v_add_u32_e32 v201, 0x1d640, v5
	ds_write_b32 v201, v200
	v_lshlrev_b32_e32 v230, 4, v3
	v_lshlrev_b32_e32 v228, 2, v182
	v_or_b32_e32 v2, s7, v229
	s_waitcnt lgkmcnt(0)
	s_barrier
	s_cmpk_lt_u32 s19, 0x100
	s_cbranch_scc1 .Llight_path
	s_setprio 1
	v_add_u32_e32 v3, 0x7800, v228
	ds_read2_b32 v[138:139], v3 offset0:16 offset1:48
	ds_read_b128 v[18:21], v2 offset:36928
	ds_read_b128 v[22:25], v2 offset:36944
	s_waitcnt lgkmcnt(2)
	v_add_u32_e32 v3, v230, v138
	ds_read_b128 v[26:29], v2 offset:36960
	ds_read_b128 v[30:33], v2 offset:36976
	ds_read_b128 v[142:145], v3 offset:16384
	ds_read_b128 v[130:133], v3 offset:16416
	ds_read_b128 v[154:157], v3 offset:16448
	ds_read_b128 v[134:137], v3 offset:16480
	ds_read_b128 v[248:251], v2 offset:37104
	ds_read_b128 v[244:247], v2 offset:37088
	ds_read_b128 v[240:243], v2 offset:37072
	ds_read_b128 v[236:239], v2 offset:37056
	s_waitcnt vmcnt(17) lgkmcnt(7)
	v_mfma_f32_32x32x16_bf16 v[18:33], v[94:97], v[142:145], v[18:33]
	s_waitcnt lgkmcnt(6)
	v_mfma_f32_32x32x16_bf16 v[18:33], v[90:93], v[130:133], v[18:33]
	s_waitcnt lgkmcnt(5)
	v_mfma_f32_32x32x16_bf16 v[18:33], v[86:89], v[154:157], v[18:33]
	s_waitcnt lgkmcnt(4)
	v_mfma_f32_32x32x16_bf16 v[18:33], v[82:85], v[134:137], v[18:33]
	s_cmpk_lt_u32 s19, 0x100
	s_cselect_b64 s[2:3], -1, 0
	ds_read_b32 v158, v228 offset:31040
	v_add_u32_e32 v159, v230, v139
	s_nop 2
	v_exp_f32_e32 v139, v20
	v_exp_f32_e32 v138, v24
	v_exp_f32_e32 v141, v28
	v_exp_f32_e32 v140, v32
	v_exp_f32_e32 v18, v18
	v_exp_f32_e32 v20, v22
	v_exp_f32_e32 v22, v26
	v_add_f32_e32 v24, 1.0, v138
	v_add_f32_e32 v26, 1.0, v141
	v_add_f32_e32 v19, 1.0, v139
	v_exp_f32_e32 v23, v30
	v_add_f32_e32 v27, 1.0, v140
	v_fmac_f32_e32 v24, v20, v24
	v_fmac_f32_e32 v26, v22, v26
	v_fmac_f32_e32 v19, v18, v19
	v_fmac_f32_e32 v27, v23, v27
	v_rcp_f32_e32 v18, v24
	v_rcp_f32_e32 v22, v27
	v_rcp_f32_e32 v19, v19
	v_rcp_f32_e32 v23, v26
	v_exp_f32_e32 v146, v21
	v_exp_f32_e32 v147, v25
	s_mov_b32 s8, 0xc038aa3b
	s_mov_b32 s4, 0x4038aa3b
	v_mov_b64_e32 v[160:161], s[8:9]
	v_exp_f32_e32 v148, v29
	v_exp_f32_e32 v149, v33
	v_pk_fma_f32 v[20:21], v[138:139], s[4:5], v[160:161] op_sel_hi:[1,0,0]
	s_nop 0
	v_pk_mul_f32 v[214:215], v[20:21], v[18:19]
	v_pk_fma_f32 v[18:19], v[140:141], s[4:5], v[160:161] op_sel_hi:[1,0,0]
	s_nop 0
	v_pk_mul_f32 v[212:213], v[18:19], v[22:23]
	v_add_u32_e32 v231, s7, v229
	ds_read_b128 v[18:21], v231 offset:36928
	ds_read_b128 v[22:25], v231 offset:36944
	ds_read_b128 v[26:29], v231 offset:36960
	ds_read_b128 v[30:33], v231 offset:36976
	s_waitcnt lgkmcnt(5)
	v_mfma_f32_32x32x16_bf16 v[2:17], v[46:49], v[142:145], v[236:251]
	ds_read_b128 v[138:141], v159 offset:16384
	v_add_f32_e32 v162, 1.0, v146
	v_exp_f32_e32 v163, v215
	v_exp_f32_e32 v164, v214
	v_exp_f32_e32 v165, v213
	v_exp_f32_e32 v166, v212
	v_add_f32_e32 v142, 1.0, v147
	v_add_f32_e32 v143, 1.0, v148
	v_add_f32_e32 v144, 1.0, v149
	v_mfma_f32_32x32x16_bf16 v[2:17], v[42:45], v[130:133], v[2:17]
	ds_read_b128 v[146:149], v159 offset:16416
	v_fmac_f32_e32 v162, v162, v163
	v_fmac_f32_e32 v142, v142, v164
	v_fmac_f32_e32 v143, v143, v165
	v_fmac_f32_e32 v144, v144, v166
	v_mfma_f32_32x32x16_bf16 v[2:17], v[38:41], v[154:157], v[2:17]
	ds_read_b128 v[150:153], v159 offset:16448
	v_rcp_f32_e32 v130, v162
	v_rcp_f32_e32 v131, v142
	v_rcp_f32_e32 v132, v143
	v_rcp_f32_e32 v133, v144
	s_waitcnt vmcnt(16)
	v_mfma_f32_32x32x16_bf16 v[2:17], v[34:37], v[134:137], v[2:17]
	ds_read_b128 v[178:181], v159 offset:16480
	v_fma_f32 v130, -v163, v130, v130
	v_fma_f32 v131, -v164, v131, v131
	v_fma_f32 v132, -v165, v132, v132
	v_fma_f32 v133, -v166, v133, v133
	v_add_u32_e32 v211, s6, v210
	v_cvt_pk_bf16_f32 v252, v130, v131
	v_cvt_pk_bf16_f32 v253, v132, v133
	s_nop 3
	v_exp_f32_e32 v131, v4
	v_exp_f32_e32 v130, v8
	v_exp_f32_e32 v133, v12
	v_exp_f32_e32 v132, v16
	v_exp_f32_e32 v2, v2
	v_exp_f32_e32 v4, v6
	v_exp_f32_e32 v6, v10
	v_exp_f32_e32 v7, v14
	v_add_f32_e32 v3, 1.0, v131
	v_add_f32_e32 v8, 1.0, v130
	v_add_f32_e32 v10, 1.0, v133
	v_add_f32_e32 v11, 1.0, v132
	v_fmac_f32_e32 v3, v2, v3
	v_fmac_f32_e32 v8, v4, v8
	v_fmac_f32_e32 v10, v6, v10
	v_fmac_f32_e32 v11, v7, v11
	v_rcp_f32_e32 v3, v3
	v_rcp_f32_e32 v2, v8
	v_rcp_f32_e32 v7, v10
	v_rcp_f32_e32 v6, v11
	v_exp_f32_e32 v134, v5
	v_exp_f32_e32 v135, v9
	v_pk_fma_f32 v[4:5], v[130:131], s[4:5], v[160:161] op_sel_hi:[1,0,0]
	v_exp_f32_e32 v130, v13
	v_pk_mul_f32 v[204:205], v[4:5], v[2:3]
	v_pk_fma_f32 v[2:3], v[132:133], s[4:5], v[160:161] op_sel_hi:[1,0,0]
	v_exp_f32_e32 v131, v17
	v_pk_mul_f32 v[202:203], v[2:3], v[6:7]
	s_waitcnt lgkmcnt(3)
	v_mfma_f32_32x32x16_bf16 v[18:33], v[94:97], v[138:141], v[18:33]
	v_add_f32_e32 v132, 1.0, v134
	v_exp_f32_e32 v133, v205
	v_add_f32_e32 v134, 1.0, v135
	v_exp_f32_e32 v135, v204
	v_exp_f32_e32 v136, v203
	v_exp_f32_e32 v137, v202
	v_add_f32_e32 v130, 1.0, v130
	v_add_f32_e32 v131, 1.0, v131
	s_waitcnt lgkmcnt(2)
	v_mfma_f32_32x32x16_bf16 v[18:33], v[90:93], v[146:149], v[18:33]
	v_fmac_f32_e32 v132, v132, v133
	v_fmac_f32_e32 v134, v134, v135
	v_fmac_f32_e32 v130, v130, v136
	v_fmac_f32_e32 v131, v131, v137
	s_waitcnt lgkmcnt(1)
	v_mfma_f32_32x32x16_bf16 v[18:33], v[86:89], v[150:153], v[18:33]
	v_rcp_f32_e32 v132, v132
	v_rcp_f32_e32 v134, v134
	v_rcp_f32_e32 v130, v130
	v_rcp_f32_e32 v131, v131
	s_waitcnt lgkmcnt(0)
	v_mfma_f32_32x32x16_bf16 v[18:33], v[82:85], v[178:181], v[18:33]
	v_fma_f32 v132, -v133, v132, v132
	v_fma_f32 v133, -v135, v134, v134
	v_fma_f32 v134, -v136, v130, v130
	v_fma_f32 v131, -v137, v131, v131
	v_cvt_pk_bf16_f32 v254, v132, v133
	v_cvt_pk_bf16_f32 v255, v134, v131
	ds_write_b128 v211, v[252:255] offset:0
	s_waitcnt lgkmcnt(0)
	s_barrier
	s_load_dwordx8 s[4:11], s[0:1], 0x10
	ds_read_b32 v194, v228 offset:31168
	ds_read_b128 v[174:177], v210
	v_add_u32_e32 v183, v230, v158
	ds_read_b128 v[170:173], v210 offset:1024
	v_exp_f32_e32 v131, v20
	v_exp_f32_e32 v130, v24
	v_exp_f32_e32 v133, v28
	v_exp_f32_e32 v132, v32
	ds_read_b128 v[166:169], v210 offset:2048
	v_exp_f32_e32 v18, v18
	v_exp_f32_e32 v20, v22
	v_exp_f32_e32 v22, v26
	v_exp_f32_e32 v23, v30
	v_add_f32_e32 v19, 1.0, v131
	v_add_f32_e32 v24, 1.0, v130
	v_add_f32_e32 v26, 1.0, v133
	v_add_f32_e32 v27, 1.0, v132
	ds_read_b128 v[162:165], v210 offset:3072
	v_fmac_f32_e32 v19, v18, v19
	v_fmac_f32_e32 v24, v20, v24
	v_fmac_f32_e32 v26, v22, v26
	v_fmac_f32_e32 v27, v23, v27
	ds_read_b128 v[158:161], v210 offset:4096
	v_rcp_f32_e32 v19, v19
	v_rcp_f32_e32 v18, v24
	v_rcp_f32_e32 v23, v26
	v_rcp_f32_e32 v22, v27
	ds_read_b128 v[154:157], v210 offset:5120
	v_exp_f32_e32 v186, v21
	v_exp_f32_e32 v187, v25
	ds_read_b128 v[142:145], v210 offset:6144
	s_mov_b32 s0, 0xc038aa3b
	s_mov_b32 s12, 0x4038aa3b
	v_mov_b64_e32 v[184:185], s[0:1]
	v_pk_fma_f32 v[20:21], v[130:131], s[12:13], v[184:185] op_sel_hi:[1,0,0]
	v_exp_f32_e32 v188, v29
	v_pk_mul_f32 v[200:201], v[20:21], v[18:19]
	v_pk_fma_f32 v[18:19], v[132:133], s[12:13], v[184:185] op_sel_hi:[1,0,0]
	v_exp_f32_e32 v189, v33
	v_pk_mul_f32 v[198:199], v[18:19], v[22:23]
	ds_read_b128 v[130:133], v210 offset:7168
	ds_read_b128 v[18:21], v231 offset:36928
	ds_read_b128 v[22:25], v231 offset:36944
	ds_read_b128 v[26:29], v231 offset:36960
	ds_read_b128 v[30:33], v231 offset:36976
	v_mfma_f32_32x32x16_bf16 v[2:17], v[46:49], v[138:141], v[236:251]
	ds_read_b128 v[134:137], v183 offset:16384
	v_add_f32_e32 v186, 1.0, v186
	v_exp_f32_e32 v190, v201
	v_exp_f32_e32 v191, v200
	v_exp_f32_e32 v192, v199
	v_exp_f32_e32 v193, v198
	v_add_f32_e32 v187, 1.0, v187
	v_add_f32_e32 v188, 1.0, v188
	v_add_f32_e32 v189, 1.0, v189
	v_mfma_f32_32x32x16_bf16 v[2:17], v[42:45], v[146:149], v[2:17]
	ds_read_b128 v[138:141], v183 offset:16416
	v_fmac_f32_e32 v186, v186, v190
	v_fmac_f32_e32 v187, v187, v191
	v_fmac_f32_e32 v188, v188, v192
	v_fmac_f32_e32 v189, v189, v193
	v_mfma_f32_32x32x16_bf16 v[2:17], v[38:41], v[150:153], v[2:17]
	ds_read_b128 v[146:149], v183 offset:16448
	v_rcp_f32_e32 v186, v186
	v_rcp_f32_e32 v187, v187
	v_rcp_f32_e32 v188, v188
	v_rcp_f32_e32 v189, v189
	v_mfma_f32_32x32x16_bf16 v[2:17], v[34:37], v[178:181], v[2:17]
	ds_read_b128 v[150:153], v183 offset:16480
	v_fma_f32 v183, -v190, v186, v186
	v_fma_f32 v186, -v191, v187, v187
	v_fma_f32 v187, -v192, v188, v188
	v_fma_f32 v188, -v193, v189, v189
	s_waitcnt vmcnt(15) lgkmcnt(0)
	v_mfma_f32_32x32x16_bf16 v[18:33], v[126:129], v[174:177], v[18:33]
	v_cvt_pk_bf16_f32 v252, v183, v186
	v_cvt_pk_bf16_f32 v253, v187, v188
	s_waitcnt vmcnt(14)
	v_mfma_f32_32x32x16_bf16 v[18:33], v[122:125], v[170:173], v[18:33]
	s_nop 0
	v_exp_f32_e32 v179, v4
	v_exp_f32_e32 v178, v8
	v_exp_f32_e32 v181, v12
	v_exp_f32_e32 v180, v16
	s_waitcnt vmcnt(13)
	v_mfma_f32_32x32x16_bf16 v[18:33], v[118:121], v[166:169], v[18:33]
	v_exp_f32_e32 v2, v2
	v_exp_f32_e32 v4, v6
	v_exp_f32_e32 v7, v10
	v_exp_f32_e32 v8, v14
	v_add_f32_e32 v3, 1.0, v179
	v_add_f32_e32 v6, 1.0, v178
	v_add_f32_e32 v10, 1.0, v181
	v_add_f32_e32 v11, 1.0, v180
	s_waitcnt vmcnt(12)
	v_mfma_f32_32x32x16_bf16 v[18:33], v[114:117], v[162:165], v[18:33]
	v_fmac_f32_e32 v3, v2, v3
	v_fmac_f32_e32 v6, v4, v6
	v_fmac_f32_e32 v10, v7, v10
	v_fmac_f32_e32 v11, v8, v11
	s_waitcnt vmcnt(11)
	v_mfma_f32_32x32x16_bf16 v[18:33], v[110:113], v[158:161], v[18:33]
	v_rcp_f32_e32 v3, v3
	v_rcp_f32_e32 v2, v6
	v_rcp_f32_e32 v7, v10
	v_rcp_f32_e32 v6, v11
	s_waitcnt vmcnt(10)
	v_mfma_f32_32x32x16_bf16 v[18:33], v[106:109], v[154:157], v[18:33]
	v_exp_f32_e32 v183, v5
	v_exp_f32_e32 v186, v9
	s_waitcnt vmcnt(9)
	v_mfma_f32_32x32x16_bf16 v[18:33], v[102:105], v[142:145], v[18:33]
	v_fma_f32 v4, v178, s12, v184
	v_fma_f32 v5, v179, s12, v184
	v_exp_f32_e32 v178, v13
	v_pk_mul_f32 v[206:207], v[4:5], v[2:3]
	v_pk_fma_f32 v[2:3], v[180:181], s[12:13], v[184:185] op_sel_hi:[1,0,0]
	v_exp_f32_e32 v179, v17
	v_pk_mul_f32 v[208:209], v[2:3], v[6:7]
	s_waitcnt vmcnt(8)
	v_mfma_f32_32x32x16_bf16 v[18:33], v[98:101], v[130:133], v[18:33]
	v_mfma_f32_32x32x16_bf16 v[18:33], v[94:97], v[134:137], v[18:33]
	v_add_f32_e32 v180, 1.0, v183
	v_exp_f32_e32 v181, v207
	v_add_f32_e32 v183, 1.0, v186
	v_exp_f32_e32 v184, v206
	v_exp_f32_e32 v185, v209
	v_exp_f32_e32 v186, v208
	v_add_f32_e32 v178, 1.0, v178
	v_add_f32_e32 v179, 1.0, v179
	v_mfma_f32_32x32x16_bf16 v[18:33], v[90:93], v[138:141], v[18:33]
	v_fmac_f32_e32 v180, v180, v181
	v_fmac_f32_e32 v183, v183, v184
	v_fmac_f32_e32 v178, v178, v185
	v_fmac_f32_e32 v179, v179, v186
	v_mfma_f32_32x32x16_bf16 v[18:33], v[86:89], v[146:149], v[18:33]
	v_rcp_f32_e32 v180, v180
	v_rcp_f32_e32 v183, v183
	v_rcp_f32_e32 v178, v178
	v_rcp_f32_e32 v179, v179
	v_mfma_f32_32x32x16_bf16 v[18:33], v[82:85], v[150:153], v[18:33]
	v_fma_f32 v180, -v181, v180, v180
	v_fma_f32 v181, -v184, v183, v183
	v_fma_f32 v183, -v185, v178, v178
	v_fma_f32 v179, -v186, v179, v179
	v_cvt_pk_bf16_f32 v254, v180, v181
	v_cvt_pk_bf16_f32 v255, v183, v179
	ds_write_b128 v211, v[252:255] offset:8192
	s_waitcnt lgkmcnt(0)
	s_barrier
	v_mov_b32_e32 v178, 0x7a40
	v_lshl_add_u32 v232, v182, 2, v178
	s_mov_b32 s1, -1
	s_branch .LBB1_14
.LBB1_13:
	v_mfma_f32_32x32x16_bf16 v[2:17], v[78:81], v[206:209], v[236:251]
	ds_read_b32 v194, v232 offset:384
	ds_read_b128 v[174:177], v210
	v_add_u32_e32 v195, v230, v233
	v_mfma_f32_32x32x16_bf16 v[2:17], v[74:77], v[190:193], v[2:17]
	ds_read_b128 v[170:173], v210 offset:1024
	v_exp_f32_e32 v199, v28
	v_exp_f32_e32 v198, v32
	v_exp_f32_e32 v197, v20
	v_exp_f32_e32 v196, v24
	v_mfma_f32_32x32x16_bf16 v[2:17], v[70:73], v[158:161], v[2:17]
	ds_read_b128 v[166:169], v210 offset:2048
	v_exp_f32_e32 v18, v18
	v_exp_f32_e32 v22, v22
	v_exp_f32_e32 v24, v26
	v_exp_f32_e32 v26, v30
	v_add_f32_e32 v20, 1.0, v197
	v_add_f32_e32 v28, 1.0, v196
	v_add_f32_e32 v30, 1.0, v199
	v_add_f32_e32 v32, 1.0, v198
	v_mfma_f32_32x32x16_bf16 v[2:17], v[66:69], v[142:145], v[2:17]
	ds_read_b128 v[162:165], v210 offset:3072
	v_exp_f32_e32 v19, v19
	v_exp_f32_e32 v23, v23
	v_exp_f32_e32 v27, v27
	v_exp_f32_e32 v31, v31
	v_fmac_f32_e32 v20, v18, v20
	v_fmac_f32_e32 v28, v22, v28
	v_fmac_f32_e32 v30, v24, v30
	v_fmac_f32_e32 v32, v26, v32
	v_mfma_f32_32x32x16_bf16 v[2:17], v[62:65], v[154:157], v[2:17]
	ds_read_b128 v[158:161], v210 offset:4096
	v_add_f32_e32 v22, 1.0, v19
	v_rcp_f32_e32 v19, v20
	v_rcp_f32_e32 v18, v28
	v_add_f32_e32 v20, 1.0, v23
	v_rcp_f32_e32 v191, v30
	v_rcp_f32_e32 v190, v32
	v_mfma_f32_32x32x16_bf16 v[2:17], v[58:61], v[182:185], v[2:17]
	ds_read_b128 v[154:157], v210 offset:5120
	v_exp_f32_e32 v206, v21
	v_exp_f32_e32 v207, v25
	v_add_f32_e32 v23, 1.0, v27
	v_rcp_f32_e32 v192, v20
	v_add_f32_e32 v20, 1.0, v31
	v_rcp_f32_e32 v193, v22
	v_mfma_f32_32x32x16_bf16 v[2:17], v[54:57], v[186:189], v[2:17]
	ds_read_b128 v[142:145], v210 offset:6144
	v_exp_f32_e32 v208, v29
	v_exp_f32_e32 v209, v33
	v_rcp_f32_e32 v183, v23
	v_rcp_f32_e32 v182, v20
	v_mfma_f32_32x32x16_bf16 v[2:17], v[50:53], v[134:137], v[2:17]
	v_mov_b64_e32 v[184:185], s[0:1]
	v_fma_f32 v20, v196, s12, v184
	v_fma_f32 v21, v197, s12, v184
	ds_read_b128 v[130:133], v210 offset:7168
	v_mul_f32_e64 v186, v20, v18
	v_mul_f32_e64 v187, v21, v19
	ds_read_b128 v[18:21], v231 offset:36928
	ds_read_b128 v[22:25], v231 offset:36944
	ds_read_b128 v[26:29], v231 offset:36960
	ds_read_b128 v[30:33], v231 offset:36976
	v_pk_fma_f32 v[134:135], v[198:199], s[12:13], v[184:185] op_sel_hi:[1,0,0]
	v_pk_fma_f32 v[200:201], v[192:193], v[220:221], v[186:187]
	v_pk_mul_f32 v[134:135], v[134:135], v[190:191]
	s_nop 0
	v_pk_fma_f32 v[198:199], v[182:183], v[222:223], v[134:135]
	v_mfma_f32_32x32x16_bf16 v[2:17], v[46:49], v[138:141], v[2:17]
	ds_read_b128 v[134:137], v195 offset:16384
	v_add_f32_e32 v182, 1.0, v206
	v_exp_f32_e32 v183, v201
	v_exp_f32_e32 v186, v200
	v_exp_f32_e32 v187, v199
	v_exp_f32_e32 v188, v198
	v_add_f32_e32 v189, 1.0, v207
	v_add_f32_e32 v190, 1.0, v208
	v_add_f32_e32 v191, 1.0, v209
	v_mfma_f32_32x32x16_bf16 v[2:17], v[42:45], v[146:149], v[2:17]
	ds_read_b128 v[138:141], v195 offset:16416
	v_fmac_f32_e32 v182, v182, v183
	v_fmac_f32_e32 v189, v189, v186
	v_fmac_f32_e32 v190, v190, v187
	v_fmac_f32_e32 v191, v191, v188
	v_mfma_f32_32x32x16_bf16 v[2:17], v[38:41], v[150:153], v[2:17]
	ds_read_b128 v[146:149], v195 offset:16448
	v_rcp_f32_e32 v182, v182
	v_rcp_f32_e32 v189, v189
	v_rcp_f32_e32 v190, v190
	v_rcp_f32_e32 v191, v191
	v_mfma_f32_32x32x16_bf16 v[2:17], v[34:37], v[178:181], v[2:17]
	ds_read_b128 v[150:153], v195 offset:16480
	v_fma_f32 v182, -v183, v182, v182
	v_fma_f32 v183, -v186, v189, v189
	v_fma_f32 v186, -v187, v190, v190
	v_fma_f32 v187, -v188, v191, v191
	s_waitcnt lgkmcnt(4)
	v_mfma_f32_32x32x16_bf16 v[18:33], v[126:129], v[174:177], v[18:33]
	v_cvt_pk_bf16_f32 v252, v182, v183
	v_cvt_pk_bf16_f32 v253, v186, v187
	v_mfma_f32_32x32x16_bf16 v[18:33], v[122:125], v[170:173], v[18:33]
	s_nop 1
	v_exp_f32_e32 v179, v4
	v_exp_f32_e32 v178, v8
	v_exp_f32_e32 v181, v12
	v_exp_f32_e32 v180, v16
	v_mfma_f32_32x32x16_bf16 v[18:33], v[118:121], v[166:169], v[18:33]
	v_exp_f32_e32 v2, v2
	v_exp_f32_e32 v6, v6
	v_exp_f32_e32 v10, v10
	v_exp_f32_e32 v12, v14
	v_add_f32_e32 v4, 1.0, v179
	v_add_f32_e32 v8, 1.0, v178
	v_add_f32_e32 v14, 1.0, v181
	v_add_f32_e32 v16, 1.0, v180
	v_mfma_f32_32x32x16_bf16 v[18:33], v[114:117], v[162:165], v[18:33]
	v_exp_f32_e32 v3, v3
	v_fmac_f32_e32 v4, v2, v4
	v_exp_f32_e32 v2, v7
	v_fmac_f32_e32 v8, v6, v8
	v_exp_f32_e32 v6, v11
	v_exp_f32_e32 v7, v15
	v_fmac_f32_e32 v14, v10, v14
	v_fmac_f32_e32 v16, v12, v16
	v_mfma_f32_32x32x16_bf16 v[18:33], v[110:113], v[158:161], v[18:33]
	v_add_f32_e32 v10, 1.0, v3
	v_rcp_f32_e32 v3, v4
	v_add_f32_e32 v4, 1.0, v2
	v_rcp_f32_e32 v2, v8
	v_rcp_f32_e32 v183, v14
	v_rcp_f32_e32 v182, v16
	v_mfma_f32_32x32x16_bf16 v[18:33], v[106:109], v[154:157], v[18:33]
	v_add_f32_e32 v6, 1.0, v6
	v_add_f32_e32 v7, 1.0, v7
	v_rcp_f32_e32 v187, v10
	v_rcp_f32_e32 v186, v4
	v_exp_f32_e32 v190, v5
	v_exp_f32_e32 v191, v9
	v_mfma_f32_32x32x16_bf16 v[18:33], v[102:105], v[142:145], v[18:33]
	v_rcp_f32_e32 v189, v6
	v_rcp_f32_e32 v188, v7
	v_exp_f32_e32 v192, v13
	v_exp_f32_e32 v193, v17
	v_pk_fma_f32 v[4:5], v[178:179], s[12:13], v[184:185] op_sel_hi:[1,0,0]
	v_mfma_f32_32x32x16_bf16 v[18:33], v[98:101], v[130:133], v[18:33]
	v_mul_f32_e64 v178, v4, v2
	v_mul_f32_e64 v179, v5, v3
	v_pk_fma_f32 v[206:207], v[186:187], v[216:217], v[178:179]
	v_pk_fma_f32 v[178:179], v[180:181], s[12:13], v[184:185] op_sel_hi:[1,0,0]
	s_nop 0
	v_pk_mul_f32 v[178:179], v[178:179], v[182:183]
	s_nop 0
	v_pk_fma_f32 v[208:209], v[188:189], v[218:219], v[178:179]
	s_waitcnt lgkmcnt(3)
	v_mfma_f32_32x32x16_bf16 v[18:33], v[94:97], v[134:137], v[18:33]
	v_add_f32_e32 v178, 1.0, v190
	v_exp_f32_e32 v179, v207
	v_add_f32_e32 v180, 1.0, v191
	v_exp_f32_e32 v181, v206
	v_exp_f32_e32 v182, v209
	v_exp_f32_e32 v183, v208
	v_add_f32_e32 v184, 1.0, v192
	v_add_f32_e32 v185, 1.0, v193
	s_waitcnt lgkmcnt(2)
	v_mfma_f32_32x32x16_bf16 v[18:33], v[90:93], v[138:141], v[18:33]
	v_fmac_f32_e32 v178, v178, v179
	v_fmac_f32_e32 v180, v180, v181
	v_fmac_f32_e32 v184, v184, v182
	v_fmac_f32_e32 v185, v185, v183
	s_waitcnt lgkmcnt(1)
	v_mfma_f32_32x32x16_bf16 v[18:33], v[86:89], v[146:149], v[18:33]
	v_rcp_f32_e32 v178, v178
	v_rcp_f32_e32 v180, v180
	v_rcp_f32_e32 v184, v184
	v_rcp_f32_e32 v185, v185
	s_waitcnt lgkmcnt(0)
	v_mfma_f32_32x32x16_bf16 v[18:33], v[82:85], v[150:153], v[18:33]
	v_fma_f32 v178, -v179, v178, v178
	v_fma_f32 v179, -v181, v180, v180
	v_fma_f32 v180, -v182, v184, v184
	v_fma_f32 v181, -v183, v185, v185
	v_cvt_pk_bf16_f32 v254, v178, v179
	v_cvt_pk_bf16_f32 v255, v180, v181
	ds_write_b128 v211, v[252:255] offset:8192
	s_waitcnt lgkmcnt(0)
	s_barrier
	s_add_i32 s1, s1, 2
	s_cmp_gt_u32 s1, 16
	v_add_u32_e32 v232, 0x200, v232
	s_cbranch_scc1 .LBB1_30
.LBB1_14:
	s_waitcnt vmcnt(7)
	v_mfma_f32_32x32x16_bf16 v[2:17], v[78:81], v[174:177], v[236:251]
	v_add_u32_e32 v192, v230, v194
	ds_read_b32 v216, v232
	ds_read_b128 v[194:197], v210 offset:8192
	s_waitcnt vmcnt(6)
	v_mfma_f32_32x32x16_bf16 v[2:17], v[74:77], v[170:173], v[2:17]
	ds_read_b128 v[178:181], v210 offset:9216
	v_exp_f32_e32 v187, v20
	v_exp_f32_e32 v186, v24
	v_exp_f32_e32 v189, v28
	v_exp_f32_e32 v188, v32
	s_waitcnt vmcnt(5)
	v_mfma_f32_32x32x16_bf16 v[2:17], v[70:73], v[166:169], v[2:17]
	ds_read_b128 v[170:173], v210 offset:10240
	v_exp_f32_e32 v18, v18
	v_exp_f32_e32 v22, v22
	v_exp_f32_e32 v24, v26
	v_exp_f32_e32 v26, v30
	v_add_f32_e32 v20, 1.0, v187
	v_add_f32_e32 v28, 1.0, v186
	v_add_f32_e32 v30, 1.0, v189
	v_add_f32_e32 v32, 1.0, v188
	s_waitcnt vmcnt(4)
	v_mfma_f32_32x32x16_bf16 v[2:17], v[66:69], v[162:165], v[2:17]
	ds_read_b128 v[166:169], v210 offset:11264
	v_exp_f32_e32 v19, v19
	v_exp_f32_e32 v23, v23
	v_exp_f32_e32 v27, v27
	v_exp_f32_e32 v31, v31
	v_fmac_f32_e32 v20, v18, v20
	v_fmac_f32_e32 v28, v22, v28
	v_fmac_f32_e32 v30, v24, v30
	v_fmac_f32_e32 v32, v26, v32
	s_waitcnt vmcnt(3)
	v_mfma_f32_32x32x16_bf16 v[2:17], v[62:65], v[158:161], v[2:17]
	ds_read_b128 v[162:165], v210 offset:12288
	v_add_f32_e32 v22, 1.0, v19
	v_rcp_f32_e32 v19, v20
	v_rcp_f32_e32 v18, v28
	v_rcp_f32_e32 v191, v30
	v_rcp_f32_e32 v190, v32
	v_add_f32_e32 v20, 1.0, v23
	s_waitcnt vmcnt(2)
	v_mfma_f32_32x32x16_bf16 v[2:17], v[58:61], v[154:157], v[2:17]
	ds_read_b128 v[174:177], v210 offset:13312
	v_rcp_f32_e32 v159, v22
	v_rcp_f32_e32 v158, v20
	v_exp_f32_e32 v160, v21
	v_exp_f32_e32 v161, v25
	v_add_f32_e32 v23, 1.0, v27
	v_add_f32_e32 v20, 1.0, v31
	s_waitcnt vmcnt(1)
	v_mfma_f32_32x32x16_bf16 v[2:17], v[54:57], v[142:145], v[2:17]
	ds_read_b128 v[182:185], v210 offset:14336
	v_rcp_f32_e32 v155, v23
	v_rcp_f32_e32 v154, v20
	v_exp_f32_e32 v193, v29
	v_exp_f32_e32 v217, v33
	s_waitcnt vmcnt(0)
	v_mfma_f32_32x32x16_bf16 v[2:17], v[50:53], v[130:133], v[2:17]
	v_mov_b64_e32 v[218:219], s[0:1]
	v_fma_f32 v20, v186, s12, v218
	v_fma_f32 v21, v187, s12, v218
	ds_read_b128 v[142:145], v210 offset:15360
	v_mul_f32_e64 v156, v20, v18
	v_mul_f32_e64 v157, v21, v19
	ds_read_b128 v[18:21], v231 offset:36928
	ds_read_b128 v[22:25], v231 offset:36944
	ds_read_b128 v[26:29], v231 offset:36960
	ds_read_b128 v[30:33], v231 offset:36976
	v_pk_fma_f32 v[130:131], v[188:189], s[12:13], v[218:219] op_sel_hi:[1,0,0]
	v_pk_fma_f32 v[214:215], v[158:159], v[214:215], v[156:157]
	v_pk_mul_f32 v[130:131], v[130:131], v[190:191]
	s_nop 0
	v_pk_fma_f32 v[212:213], v[154:155], v[212:213], v[130:131]
	v_mfma_f32_32x32x16_bf16 v[2:17], v[46:49], v[134:137], v[2:17]
	ds_read_b128 v[154:157], v192 offset:16384
	v_add_f32_e32 v130, 1.0, v160
	v_exp_f32_e32 v131, v215
	v_exp_f32_e32 v132, v214
	v_exp_f32_e32 v133, v213
	v_exp_f32_e32 v220, v212
	v_add_f32_e32 v134, 1.0, v161
	v_add_f32_e32 v135, 1.0, v193
	v_add_f32_e32 v136, 1.0, v217
	v_mfma_f32_32x32x16_bf16 v[2:17], v[42:45], v[138:141], v[2:17]
	ds_read_b128 v[158:161], v192 offset:16416
	v_fmac_f32_e32 v130, v130, v131
	v_fmac_f32_e32 v134, v134, v132
	v_fmac_f32_e32 v135, v135, v133
	v_fmac_f32_e32 v136, v136, v220
	v_mfma_f32_32x32x16_bf16 v[2:17], v[38:41], v[146:149], v[2:17]
	ds_read_b128 v[186:189], v192 offset:16448
	v_rcp_f32_e32 v130, v130
	v_rcp_f32_e32 v134, v134
	v_rcp_f32_e32 v135, v135
	v_rcp_f32_e32 v136, v136
	v_mfma_f32_32x32x16_bf16 v[2:17], v[34:37], v[150:153], v[2:17]
	ds_read_b128 v[190:193], v192 offset:16480
	v_fma_f32 v130, -v131, v130, v130
	v_fma_f32 v131, -v132, v134, v134
	v_fma_f32 v132, -v133, v135, v135
	v_fma_f32 v133, -v220, v136, v136
	s_waitcnt lgkmcnt(4)
	v_mfma_f32_32x32x16_bf16 v[18:33], v[126:129], v[194:197], v[18:33]
	v_cvt_pk_bf16_f32 v252, v130, v131
	v_cvt_pk_bf16_f32 v253, v132, v133
	v_mfma_f32_32x32x16_bf16 v[18:33], v[122:125], v[178:181], v[18:33]
	s_nop 1
	v_exp_f32_e32 v131, v4
	v_exp_f32_e32 v130, v8
	v_exp_f32_e32 v133, v12
	v_exp_f32_e32 v132, v16
	v_mfma_f32_32x32x16_bf16 v[18:33], v[118:121], v[170:173], v[18:33]
	v_exp_f32_e32 v2, v2
	v_exp_f32_e32 v6, v6
	v_exp_f32_e32 v10, v10
	v_exp_f32_e32 v12, v14
	v_add_f32_e32 v4, 1.0, v131
	v_add_f32_e32 v8, 1.0, v130
	v_add_f32_e32 v14, 1.0, v133
	v_add_f32_e32 v16, 1.0, v132
	v_mfma_f32_32x32x16_bf16 v[18:33], v[114:117], v[166:169], v[18:33]
	v_exp_f32_e32 v3, v3
	v_fmac_f32_e32 v4, v2, v4
	v_exp_f32_e32 v2, v7
	v_fmac_f32_e32 v8, v6, v8
	v_exp_f32_e32 v6, v11
	v_exp_f32_e32 v7, v15
	v_fmac_f32_e32 v14, v10, v14
	v_fmac_f32_e32 v16, v12, v16
	v_mfma_f32_32x32x16_bf16 v[18:33], v[110:113], v[162:165], v[18:33]
	v_add_f32_e32 v10, 1.0, v3
	v_rcp_f32_e32 v3, v4
	v_add_f32_e32 v4, 1.0, v2
	v_rcp_f32_e32 v2, v8
	v_rcp_f32_e32 v135, v14
	v_rcp_f32_e32 v134, v16
	v_mfma_f32_32x32x16_bf16 v[18:33], v[106:109], v[174:177], v[18:33]
	v_add_f32_e32 v6, 1.0, v6
	v_add_f32_e32 v7, 1.0, v7
	v_rcp_f32_e32 v137, v10
	v_rcp_f32_e32 v136, v4
	v_exp_f32_e32 v140, v5
	v_exp_f32_e32 v141, v9
	v_mfma_f32_32x32x16_bf16 v[18:33], v[102:105], v[182:185], v[18:33]
	v_rcp_f32_e32 v139, v6
	v_rcp_f32_e32 v138, v7
	v_exp_f32_e32 v146, v13
	v_exp_f32_e32 v147, v17
	v_pk_fma_f32 v[4:5], v[130:131], s[12:13], v[218:219] op_sel_hi:[1,0,0]
	v_mfma_f32_32x32x16_bf16 v[18:33], v[98:101], v[142:145], v[18:33]
	v_mul_f32_e64 v130, v4, v2
	v_mul_f32_e64 v131, v5, v3
	v_pk_fma_f32 v[224:225], v[136:137], v[204:205], v[130:131]
	v_pk_fma_f32 v[130:131], v[132:133], s[12:13], v[218:219] op_sel_hi:[1,0,0]
	s_nop 0
	v_pk_mul_f32 v[130:131], v[130:131], v[134:135]
	s_nop 0
	v_pk_fma_f32 v[226:227], v[138:139], v[202:203], v[130:131]
	s_waitcnt lgkmcnt(3)
	v_mfma_f32_32x32x16_bf16 v[18:33], v[94:97], v[154:157], v[18:33]
	v_add_f32_e32 v130, 1.0, v140
	v_exp_f32_e32 v131, v225
	v_add_f32_e32 v132, 1.0, v141
	v_exp_f32_e32 v133, v224
	v_exp_f32_e32 v134, v227
	v_exp_f32_e32 v135, v226
	v_add_f32_e32 v136, 1.0, v146
	v_add_f32_e32 v137, 1.0, v147
	s_waitcnt lgkmcnt(2)
	v_mfma_f32_32x32x16_bf16 v[18:33], v[90:93], v[158:161], v[18:33]
	v_fmac_f32_e32 v130, v130, v131
	v_fmac_f32_e32 v132, v132, v133
	v_fmac_f32_e32 v136, v136, v134
	v_fmac_f32_e32 v137, v137, v135
	s_waitcnt lgkmcnt(1)
	v_mfma_f32_32x32x16_bf16 v[18:33], v[86:89], v[186:189], v[18:33]
	v_rcp_f32_e32 v130, v130
	v_rcp_f32_e32 v132, v132
	v_rcp_f32_e32 v136, v136
	v_rcp_f32_e32 v137, v137
	s_waitcnt lgkmcnt(0)
	v_mfma_f32_32x32x16_bf16 v[18:33], v[82:85], v[190:193], v[18:33]
	v_fma_f32 v130, -v131, v130, v130
	v_fma_f32 v131, -v133, v132, v132
	v_fma_f32 v132, -v134, v136, v136
	v_fma_f32 v133, -v135, v137, v137
	v_cvt_pk_bf16_f32 v254, v130, v131
	v_cvt_pk_bf16_f32 v255, v132, v133
	ds_write_b128 v211, v[252:255] offset:0
	s_waitcnt lgkmcnt(0)
	s_barrier
	v_mfma_f32_32x32x16_bf16 v[2:17], v[78:81], v[194:197], v[236:251]
	ds_read_b32 v233, v232 offset:128
	ds_read_b128 v[202:205], v210
	v_add_u32_e32 v216, v230, v216
	v_mfma_f32_32x32x16_bf16 v[2:17], v[74:77], v[178:181], v[2:17]
	ds_read_b128 v[194:197], v210 offset:1024
	v_exp_f32_e32 v147, v20
	v_exp_f32_e32 v146, v24
	v_exp_f32_e32 v149, v28
	v_exp_f32_e32 v148, v32
	v_mfma_f32_32x32x16_bf16 v[2:17], v[70:73], v[170:173], v[2:17]
	ds_read_b128 v[138:141], v210 offset:2048
	v_exp_f32_e32 v18, v18
	v_exp_f32_e32 v22, v22
	v_exp_f32_e32 v24, v26
	v_exp_f32_e32 v26, v30
	v_add_f32_e32 v20, 1.0, v147
	v_add_f32_e32 v28, 1.0, v146
	v_add_f32_e32 v30, 1.0, v149
	v_add_f32_e32 v32, 1.0, v148
	v_mfma_f32_32x32x16_bf16 v[2:17], v[66:69], v[166:169], v[2:17]
	ds_read_b128 v[134:137], v210 offset:3072
	v_exp_f32_e32 v19, v19
	v_exp_f32_e32 v23, v23
	v_exp_f32_e32 v27, v27
	v_exp_f32_e32 v31, v31
	v_fmac_f32_e32 v20, v18, v20
	v_fmac_f32_e32 v28, v22, v28
	v_fmac_f32_e32 v30, v24, v30
	v_fmac_f32_e32 v32, v26, v32
	v_mfma_f32_32x32x16_bf16 v[2:17], v[62:65], v[162:165], v[2:17]
	ds_read_b128 v[166:169], v210 offset:4096
	v_add_f32_e32 v22, 1.0, v19
	v_rcp_f32_e32 v19, v20
	v_rcp_f32_e32 v18, v28
	v_rcp_f32_e32 v151, v30
	v_rcp_f32_e32 v150, v32
	v_add_f32_e32 v20, 1.0, v23
	v_mfma_f32_32x32x16_bf16 v[2:17], v[58:61], v[174:177], v[2:17]
	ds_read_b128 v[162:165], v210 offset:5120
	v_rcp_f32_e32 v153, v22
	v_rcp_f32_e32 v152, v20
	v_add_f32_e32 v23, 1.0, v27
	v_add_f32_e32 v20, 1.0, v31
	v_exp_f32_e32 v180, v21
	v_exp_f32_e32 v181, v25
	v_mfma_f32_32x32x16_bf16 v[2:17], v[54:57], v[182:185], v[2:17]
	ds_read_b128 v[170:173], v210 offset:6144
	v_rcp_f32_e32 v175, v23
	v_rcp_f32_e32 v174, v20
	v_exp_f32_e32 v176, v29
	v_exp_f32_e32 v177, v33
	v_mfma_f32_32x32x16_bf16 v[2:17], v[50:53], v[142:145], v[2:17]
	v_mov_b64_e32 v[178:179], s[0:1]
	v_fma_f32 v20, v146, s12, v178
	v_fma_f32 v21, v147, s12, v178
	ds_read_b128 v[130:133], v210 offset:7168
	v_mul_f32_e64 v146, v20, v18
	v_mul_f32_e64 v147, v21, v19
	ds_read_b128 v[18:21], v231 offset:36928
	ds_read_b128 v[22:25], v231 offset:36944
	ds_read_b128 v[26:29], v231 offset:36960
	ds_read_b128 v[30:33], v231 offset:36976
	v_pk_fma_f32 v[142:143], v[148:149], s[12:13], v[178:179] op_sel_hi:[1,0,0]
	v_pk_fma_f32 v[220:221], v[152:153], v[200:201], v[146:147]
	v_pk_mul_f32 v[142:143], v[142:143], v[150:151]
	s_nop 0
	v_pk_fma_f32 v[222:223], v[174:175], v[198:199], v[142:143]
	v_mfma_f32_32x32x16_bf16 v[2:17], v[46:49], v[154:157], v[2:17]
	ds_read_b128 v[146:149], v216 offset:16384
	v_add_f32_e32 v142, 1.0, v180
	v_exp_f32_e32 v143, v221
	v_exp_f32_e32 v144, v220
	v_exp_f32_e32 v145, v223
	v_exp_f32_e32 v180, v222
	v_add_f32_e32 v154, 1.0, v181
	v_add_f32_e32 v155, 1.0, v176
	v_add_f32_e32 v156, 1.0, v177
	v_mfma_f32_32x32x16_bf16 v[2:17], v[42:45], v[158:161], v[2:17]
	ds_read_b128 v[150:153], v216 offset:16416
	v_fmac_f32_e32 v142, v142, v143
	v_fmac_f32_e32 v154, v154, v144
	v_fmac_f32_e32 v155, v155, v145
	v_fmac_f32_e32 v156, v156, v180
	v_mfma_f32_32x32x16_bf16 v[2:17], v[38:41], v[186:189], v[2:17]
	ds_read_b128 v[174:177], v216 offset:16448
	v_rcp_f32_e32 v142, v142
	v_rcp_f32_e32 v154, v154
	v_rcp_f32_e32 v155, v155
	v_rcp_f32_e32 v156, v156
	v_mfma_f32_32x32x16_bf16 v[2:17], v[34:37], v[190:193], v[2:17]
	ds_read_b128 v[198:201], v216 offset:16480
	v_fma_f32 v142, -v143, v142, v142
	v_fma_f32 v143, -v144, v154, v154
	v_fma_f32 v144, -v145, v155, v155
	v_fma_f32 v145, -v180, v156, v156
	s_waitcnt lgkmcnt(4)
	v_mfma_f32_32x32x16_bf16 v[18:33], v[126:129], v[202:205], v[18:33]
	v_cvt_pk_bf16_f32 v252, v142, v143
	v_cvt_pk_bf16_f32 v253, v144, v145
	v_mfma_f32_32x32x16_bf16 v[18:33], v[122:125], v[194:197], v[18:33]
	s_nop 1
	v_exp_f32_e32 v143, v4
	v_exp_f32_e32 v142, v8
	v_exp_f32_e32 v145, v12
	v_exp_f32_e32 v144, v16
	v_mfma_f32_32x32x16_bf16 v[18:33], v[118:121], v[138:141], v[18:33]
	v_exp_f32_e32 v2, v2
	v_exp_f32_e32 v6, v6
	v_exp_f32_e32 v10, v10
	v_exp_f32_e32 v12, v14
	v_add_f32_e32 v4, 1.0, v143
	v_add_f32_e32 v8, 1.0, v142
	v_add_f32_e32 v14, 1.0, v145
	v_add_f32_e32 v16, 1.0, v144
	v_mfma_f32_32x32x16_bf16 v[18:33], v[114:117], v[134:137], v[18:33]
	v_exp_f32_e32 v3, v3
	v_fmac_f32_e32 v4, v2, v4
	v_exp_f32_e32 v2, v7
	v_fmac_f32_e32 v8, v6, v8
	v_exp_f32_e32 v6, v11
	v_exp_f32_e32 v7, v15
	v_fmac_f32_e32 v14, v10, v14
	v_fmac_f32_e32 v16, v12, v16
	v_mfma_f32_32x32x16_bf16 v[18:33], v[110:113], v[166:169], v[18:33]
	v_add_f32_e32 v10, 1.0, v3
	v_rcp_f32_e32 v3, v4
	v_add_f32_e32 v4, 1.0, v2
	v_rcp_f32_e32 v2, v8
	v_rcp_f32_e32 v155, v14
	v_rcp_f32_e32 v154, v16
	v_mfma_f32_32x32x16_bf16 v[18:33], v[106:109], v[162:165], v[18:33]
	v_add_f32_e32 v6, 1.0, v6
	v_add_f32_e32 v7, 1.0, v7
	v_rcp_f32_e32 v157, v10
	v_rcp_f32_e32 v156, v4
	v_exp_f32_e32 v160, v5
	v_exp_f32_e32 v161, v9
	v_mfma_f32_32x32x16_bf16 v[18:33], v[102:105], v[170:173], v[18:33]
	v_rcp_f32_e32 v159, v6
	v_rcp_f32_e32 v158, v7
	v_exp_f32_e32 v180, v13
	v_exp_f32_e32 v181, v17
	v_pk_fma_f32 v[4:5], v[142:143], s[12:13], v[178:179] op_sel_hi:[1,0,0]
	v_mfma_f32_32x32x16_bf16 v[18:33], v[98:101], v[130:133], v[18:33]
	v_mul_f32_e64 v142, v4, v2
	v_mul_f32_e64 v143, v5, v3
	v_pk_fma_f32 v[216:217], v[156:157], v[206:207], v[142:143]
	v_pk_fma_f32 v[142:143], v[144:145], s[12:13], v[178:179] op_sel_hi:[1,0,0]
	s_nop 0
	v_pk_mul_f32 v[142:143], v[142:143], v[154:155]
	s_nop 0
	v_pk_fma_f32 v[218:219], v[158:159], v[208:209], v[142:143]
	s_waitcnt lgkmcnt(3)
	v_mfma_f32_32x32x16_bf16 v[18:33], v[94:97], v[146:149], v[18:33]
	v_add_f32_e32 v142, 1.0, v160
	v_exp_f32_e32 v143, v217
	v_add_f32_e32 v144, 1.0, v161
	v_exp_f32_e32 v145, v216
	v_exp_f32_e32 v154, v219
	v_exp_f32_e32 v155, v218
	v_add_f32_e32 v156, 1.0, v180
	v_add_f32_e32 v157, 1.0, v181
	s_waitcnt lgkmcnt(2)
	v_mfma_f32_32x32x16_bf16 v[18:33], v[90:93], v[150:153], v[18:33]
	v_fmac_f32_e32 v142, v142, v143
	v_fmac_f32_e32 v144, v144, v145
	v_fmac_f32_e32 v156, v156, v154
	v_fmac_f32_e32 v157, v157, v155
	s_waitcnt lgkmcnt(1)
	v_mfma_f32_32x32x16_bf16 v[18:33], v[86:89], v[174:177], v[18:33]
	v_rcp_f32_e32 v142, v142
	v_rcp_f32_e32 v144, v144
	v_rcp_f32_e32 v156, v156
	v_rcp_f32_e32 v157, v157
	s_waitcnt lgkmcnt(0)
	v_mfma_f32_32x32x16_bf16 v[18:33], v[82:85], v[198:201], v[18:33]
	v_fma_f32 v142, -v143, v142, v142
	v_fma_f32 v143, -v145, v144, v144
	v_fma_f32 v144, -v154, v156, v156
	v_fma_f32 v145, -v155, v157, v157
	v_cvt_pk_bf16_f32 v254, v142, v143
	v_cvt_pk_bf16_f32 v255, v144, v145
	ds_write_b128 v211, v[252:255] offset:8192
	s_waitcnt lgkmcnt(0)
	s_barrier
	v_mfma_f32_32x32x16_bf16 v[2:17], v[78:81], v[202:205], v[236:251]
	v_add_u32_e32 v234, v230, v233
	ds_read_b32 v233, v232 offset:256
	ds_read_b128 v[206:209], v210 offset:8192
	v_mfma_f32_32x32x16_bf16 v[2:17], v[74:77], v[194:197], v[2:17]
	ds_read_b128 v[190:193], v210 offset:9216
	v_exp_f32_e32 v179, v20
	v_exp_f32_e32 v178, v24
	v_exp_f32_e32 v181, v28
	v_exp_f32_e32 v180, v32
	v_mfma_f32_32x32x16_bf16 v[2:17], v[70:73], v[138:141], v[2:17]
	ds_read_b128 v[158:161], v210 offset:10240
	v_exp_f32_e32 v18, v18
	v_exp_f32_e32 v22, v22
	v_exp_f32_e32 v24, v26
	v_exp_f32_e32 v26, v30
	v_add_f32_e32 v20, 1.0, v179
	v_add_f32_e32 v28, 1.0, v178
	v_add_f32_e32 v30, 1.0, v181
	v_add_f32_e32 v32, 1.0, v180
	v_mfma_f32_32x32x16_bf16 v[2:17], v[66:69], v[134:137], v[2:17]
	ds_read_b128 v[142:145], v210 offset:11264
	v_exp_f32_e32 v19, v19
	v_exp_f32_e32 v23, v23
	v_exp_f32_e32 v27, v27
	v_exp_f32_e32 v31, v31
	v_fmac_f32_e32 v20, v18, v20
	v_fmac_f32_e32 v28, v22, v28
	v_fmac_f32_e32 v30, v24, v30
	v_fmac_f32_e32 v32, v26, v32
	v_mfma_f32_32x32x16_bf16 v[2:17], v[62:65], v[166:169], v[2:17]
	ds_read_b128 v[154:157], v210 offset:12288
	v_add_f32_e32 v22, 1.0, v19
	v_rcp_f32_e32 v19, v20
	v_rcp_f32_e32 v18, v28
	v_rcp_f32_e32 v139, v30
	v_rcp_f32_e32 v138, v32
	v_add_f32_e32 v20, 1.0, v23
	v_mfma_f32_32x32x16_bf16 v[2:17], v[58:61], v[162:165], v[2:17]
	ds_read_b128 v[182:185], v210 offset:13312
	v_rcp_f32_e32 v141, v22
	v_rcp_f32_e32 v140, v20
	v_add_f32_e32 v23, 1.0, v27
	v_add_f32_e32 v20, 1.0, v31
	v_exp_f32_e32 v168, v21
	v_exp_f32_e32 v169, v25
	v_mfma_f32_32x32x16_bf16 v[2:17], v[54:57], v[170:173], v[2:17]
	ds_read_b128 v[186:189], v210 offset:14336
	v_rcp_f32_e32 v163, v23
	v_rcp_f32_e32 v162, v20
	v_exp_f32_e32 v194, v29
	v_exp_f32_e32 v195, v33
	v_mfma_f32_32x32x16_bf16 v[2:17], v[50:53], v[130:133], v[2:17]
	v_mov_b64_e32 v[164:165], s[0:1]
	v_fma_f32 v20, v178, s12, v164
	v_fma_f32 v21, v179, s12, v164
	ds_read_b128 v[134:137], v210 offset:15360
	v_mul_f32_e64 v166, v20, v18
	v_mul_f32_e64 v167, v21, v19
	ds_read_b128 v[18:21], v231 offset:36928
	ds_read_b128 v[22:25], v231 offset:36944
	ds_read_b128 v[26:29], v231 offset:36960
	ds_read_b128 v[30:33], v231 offset:36976
	v_pk_fma_f32 v[130:131], v[180:181], s[12:13], v[164:165] op_sel_hi:[1,0,0]
	v_pk_fma_f32 v[214:215], v[140:141], v[214:215], v[166:167]
	v_pk_mul_f32 v[130:131], v[130:131], v[138:139]
	s_nop 0
	v_pk_fma_f32 v[212:213], v[162:163], v[212:213], v[130:131]
	v_mfma_f32_32x32x16_bf16 v[2:17], v[46:49], v[146:149], v[2:17]
	ds_read_b128 v[138:141], v234 offset:16384
	v_add_f32_e32 v130, 1.0, v168
	v_exp_f32_e32 v131, v215
	v_exp_f32_e32 v132, v214
	v_exp_f32_e32 v133, v213
	v_exp_f32_e32 v162, v212
	v_add_f32_e32 v163, 1.0, v169
	v_add_f32_e32 v166, 1.0, v194
	v_add_f32_e32 v167, 1.0, v195
	v_mfma_f32_32x32x16_bf16 v[2:17], v[42:45], v[150:153], v[2:17]
	ds_read_b128 v[146:149], v234 offset:16416
	v_fmac_f32_e32 v130, v130, v131
	v_fmac_f32_e32 v163, v163, v132
	v_fmac_f32_e32 v166, v166, v133
	v_fmac_f32_e32 v167, v167, v162
	v_mfma_f32_32x32x16_bf16 v[2:17], v[38:41], v[174:177], v[2:17]
	ds_read_b128 v[150:153], v234 offset:16448
	v_rcp_f32_e32 v130, v130
	v_rcp_f32_e32 v163, v163
	v_rcp_f32_e32 v166, v166
	v_rcp_f32_e32 v167, v167
	v_mfma_f32_32x32x16_bf16 v[2:17], v[34:37], v[198:201], v[2:17]
	ds_read_b128 v[178:181], v234 offset:16480
	v_fma_f32 v130, -v131, v130, v130
	v_fma_f32 v131, -v132, v163, v163
	v_fma_f32 v132, -v133, v166, v166
	v_fma_f32 v133, -v162, v167, v167
	s_waitcnt lgkmcnt(4)
	v_mfma_f32_32x32x16_bf16 v[18:33], v[126:129], v[206:209], v[18:33]
	v_cvt_pk_bf16_f32 v252, v130, v131
	v_cvt_pk_bf16_f32 v253, v132, v133
	v_mfma_f32_32x32x16_bf16 v[18:33], v[122:125], v[190:193], v[18:33]
	s_nop 1
	v_exp_f32_e32 v131, v4
	v_exp_f32_e32 v130, v8
	v_exp_f32_e32 v133, v12
	v_exp_f32_e32 v132, v16
	v_mfma_f32_32x32x16_bf16 v[18:33], v[118:121], v[158:161], v[18:33]
	v_exp_f32_e32 v2, v2
	v_exp_f32_e32 v6, v6
	v_exp_f32_e32 v10, v10
	v_exp_f32_e32 v12, v14
	v_add_f32_e32 v4, 1.0, v131
	v_add_f32_e32 v8, 1.0, v130
	v_add_f32_e32 v14, 1.0, v133
	v_add_f32_e32 v16, 1.0, v132
	v_mfma_f32_32x32x16_bf16 v[18:33], v[114:117], v[142:145], v[18:33]
	v_exp_f32_e32 v3, v3
	v_fmac_f32_e32 v4, v2, v4
	v_exp_f32_e32 v2, v7
	v_fmac_f32_e32 v8, v6, v8
	v_exp_f32_e32 v6, v11
	v_exp_f32_e32 v7, v15
	v_fmac_f32_e32 v14, v10, v14
	v_fmac_f32_e32 v16, v12, v16
	v_mfma_f32_32x32x16_bf16 v[18:33], v[110:113], v[154:157], v[18:33]
	v_add_f32_e32 v10, 1.0, v3
	v_rcp_f32_e32 v3, v4
	v_add_f32_e32 v4, 1.0, v2
	v_rcp_f32_e32 v2, v8
	v_rcp_f32_e32 v163, v14
	v_rcp_f32_e32 v162, v16
	v_mfma_f32_32x32x16_bf16 v[18:33], v[106:109], v[182:185], v[18:33]
	v_add_f32_e32 v6, 1.0, v6
	v_add_f32_e32 v7, 1.0, v7
	v_rcp_f32_e32 v167, v10
	v_rcp_f32_e32 v166, v4
	v_exp_f32_e32 v170, v5
	v_exp_f32_e32 v171, v9
	v_mfma_f32_32x32x16_bf16 v[18:33], v[102:105], v[186:189], v[18:33]
	v_rcp_f32_e32 v169, v6
	v_rcp_f32_e32 v168, v7
	v_exp_f32_e32 v172, v13
	v_exp_f32_e32 v173, v17
	v_pk_fma_f32 v[4:5], v[130:131], s[12:13], v[164:165] op_sel_hi:[1,0,0]
	v_mfma_f32_32x32x16_bf16 v[18:33], v[98:101], v[134:137], v[18:33]
	v_mul_f32_e64 v130, v4, v2
	v_mul_f32_e64 v131, v5, v3
	v_pk_fma_f32 v[204:205], v[166:167], v[224:225], v[130:131]
	v_pk_fma_f32 v[130:131], v[132:133], s[12:13], v[164:165] op_sel_hi:[1,0,0]
	s_nop 0
	v_pk_mul_f32 v[130:131], v[130:131], v[162:163]
	s_nop 0
	v_pk_fma_f32 v[202:203], v[168:169], v[226:227], v[130:131]
	s_waitcnt lgkmcnt(3)
	v_mfma_f32_32x32x16_bf16 v[18:33], v[94:97], v[138:141], v[18:33]
	v_add_f32_e32 v130, 1.0, v170
	v_exp_f32_e32 v131, v205
	v_add_f32_e32 v132, 1.0, v171
	v_exp_f32_e32 v133, v204
	v_exp_f32_e32 v162, v203
	v_exp_f32_e32 v163, v202
	v_add_f32_e32 v164, 1.0, v172
	v_add_f32_e32 v165, 1.0, v173
	s_waitcnt lgkmcnt(2)
	v_mfma_f32_32x32x16_bf16 v[18:33], v[90:93], v[146:149], v[18:33]
	v_fmac_f32_e32 v130, v130, v131
	v_fmac_f32_e32 v132, v132, v133
	v_fmac_f32_e32 v164, v164, v162
	v_fmac_f32_e32 v165, v165, v163
	s_waitcnt lgkmcnt(1)
	v_mfma_f32_32x32x16_bf16 v[18:33], v[86:89], v[150:153], v[18:33]
	v_rcp_f32_e32 v130, v130
	v_rcp_f32_e32 v132, v132
	v_rcp_f32_e32 v164, v164
	v_rcp_f32_e32 v165, v165
	s_waitcnt lgkmcnt(0)
	v_mfma_f32_32x32x16_bf16 v[18:33], v[82:85], v[178:181], v[18:33]
	v_fma_f32 v130, -v131, v130, v130
	v_fma_f32 v131, -v133, v132, v132
	v_fma_f32 v132, -v162, v164, v164
	v_fma_f32 v133, -v163, v165, v165
	v_cvt_pk_bf16_f32 v254, v130, v131
	v_cvt_pk_bf16_f32 v255, v132, v133
	ds_write_b128 v211, v[252:255] offset:0
	s_waitcnt lgkmcnt(0)
	s_barrier
	s_branch .LBB1_13
.LBB1_30:
	v_mfma_f32_32x32x16_bf16 v[2:17], v[78:81], v[174:177], v[236:251]
	ds_read_b128 v[178:181], v210 offset:8192
	v_add_u32_e32 v182, v230, v194
	v_mfma_f32_32x32x16_bf16 v[2:17], v[74:77], v[170:173], v[2:17]
	ds_read_b128 v[174:177], v210 offset:9216
	v_exp_f32_e32 v20, v20
	v_exp_f32_e32 v24, v24
	v_exp_f32_e32 v28, v28
	v_exp_f32_e32 v32, v32
	v_mfma_f32_32x32x16_bf16 v[2:17], v[70:73], v[166:169], v[2:17]
	ds_read_b128 v[170:173], v210 offset:10240
	v_exp_f32_e32 v18, v18
	v_exp_f32_e32 v22, v22
	v_exp_f32_e32 v26, v26
	v_exp_f32_e32 v30, v30
	v_add_f32_e32 v183, 1.0, v20
	v_add_f32_e32 v184, 1.0, v24
	v_add_f32_e32 v185, 1.0, v28
	v_add_f32_e32 v186, 1.0, v32
	v_mfma_f32_32x32x16_bf16 v[2:17], v[66:69], v[162:165], v[2:17]
	ds_read_b128 v[166:169], v210 offset:11264
	v_exp_f32_e32 v19, v19
	v_fmac_f32_e32 v183, v18, v183
	v_exp_f32_e32 v18, v23
	v_exp_f32_e32 v23, v27
	v_exp_f32_e32 v27, v31
	v_fmac_f32_e32 v184, v22, v184
	v_fmac_f32_e32 v185, v26, v185
	v_fmac_f32_e32 v186, v30, v186
	v_mfma_f32_32x32x16_bf16 v[2:17], v[62:65], v[158:161], v[2:17]
	ds_read_b128 v[162:165], v210 offset:12288
	v_rcp_f32_e32 v22, v183
	v_rcp_f32_e32 v26, v184
	v_rcp_f32_e32 v30, v185
	v_rcp_f32_e32 v31, v186
	v_mov_b32_e32 v183, 0xc038aa3b
	v_add_f32_e32 v19, 1.0, v19
	v_fmamk_f32 v20, v20, 0x4038aa3b, v183
	v_add_f32_e32 v18, 1.0, v18
	v_fmamk_f32 v24, v24, 0x4038aa3b, v183
	v_mfma_f32_32x32x16_bf16 v[2:17], v[58:61], v[154:157], v[2:17]
	ds_read_b128 v[158:161], v210 offset:13312
	v_rcp_f32_e32 v19, v19
	v_add_f32_e32 v23, 1.0, v23
	v_rcp_f32_e32 v184, v18
	v_exp_f32_e32 v185, v21
	v_exp_f32_e32 v186, v25
	v_fmamk_f32 v18, v28, 0x4038aa3b, v183
	v_add_f32_e32 v21, 1.0, v27
	v_fmamk_f32 v25, v32, 0x4038aa3b, v183
	v_mfma_f32_32x32x16_bf16 v[2:17], v[54:57], v[142:145], v[2:17]
	ds_read_b128 v[154:157], v210 offset:14336
	v_mul_f32_e32 v187, v20, v22
	v_rcp_f32_e32 v188, v23
	v_rcp_f32_e32 v189, v21
	v_exp_f32_e32 v190, v29
	v_exp_f32_e32 v191, v33
	v_mul_f32_e32 v192, v24, v26
	v_mul_f32_e32 v193, v18, v30
	v_mul_f32_e32 v194, v25, v31
	v_mfma_f32_32x32x16_bf16 v[2:17], v[50:53], v[130:133], v[2:17]
	ds_read_b128 v[142:145], v210 offset:15360
	v_fmac_f32_e32 v187, v19, v215
	ds_read_b128 v[18:21], v231 offset:36928
	ds_read_b128 v[22:25], v231 offset:36944
	ds_read_b128 v[26:29], v231 offset:36960
	ds_read_b128 v[30:33], v231 offset:36976
	v_fmac_f32_e32 v192, v184, v214
	v_fmac_f32_e32 v193, v188, v213
	v_fmac_f32_e32 v194, v189, v212
	v_mfma_f32_32x32x16_bf16 v[2:17], v[46:49], v[134:137], v[2:17]
	ds_read_b128 v[130:133], v182 offset:16384
	v_add_f32_e32 v184, 1.0, v185
	v_exp_f32_e32 v185, v187
	v_exp_f32_e32 v187, v192
	v_exp_f32_e32 v188, v193
	v_exp_f32_e32 v189, v194
	v_add_f32_e32 v186, 1.0, v186
	v_add_f32_e32 v190, 1.0, v190
	v_add_f32_e32 v191, 1.0, v191
	v_mfma_f32_32x32x16_bf16 v[2:17], v[42:45], v[138:141], v[2:17]
	ds_read_b128 v[134:137], v182 offset:16416
	v_fmac_f32_e32 v184, v184, v185
	v_fmac_f32_e32 v186, v186, v187
	v_fmac_f32_e32 v190, v190, v188
	v_fmac_f32_e32 v191, v191, v189
	v_mfma_f32_32x32x16_bf16 v[2:17], v[38:41], v[146:149], v[2:17]
	ds_read_b128 v[138:141], v182 offset:16448
	v_rcp_f32_e32 v184, v184
	v_rcp_f32_e32 v186, v186
	v_rcp_f32_e32 v190, v190
	v_rcp_f32_e32 v191, v191
	v_mfma_f32_32x32x16_bf16 v[2:17], v[34:37], v[150:153], v[2:17]
	ds_read_b128 v[146:149], v182 offset:16480
	v_fma_f32 v182, -v185, v184, v184
	v_fma_f32 v184, -v187, v186, v186
	v_fma_f32 v185, -v188, v190, v190
	v_fma_f32 v186, -v189, v191, v191
	s_waitcnt lgkmcnt(4)
	v_mfma_f32_32x32x16_bf16 v[18:33], v[126:129], v[178:181], v[18:33]
	v_cvt_pk_bf16_f32 v252, v182, v184
	v_cvt_pk_bf16_f32 v253, v185, v186
	v_mfma_f32_32x32x16_bf16 v[18:33], v[122:125], v[174:177], v[18:33]
	s_nop 1
	v_exp_f32_e32 v4, v4
	v_exp_f32_e32 v8, v8
	v_exp_f32_e32 v12, v12
	v_exp_f32_e32 v16, v16
	v_mfma_f32_32x32x16_bf16 v[18:33], v[118:121], v[170:173], v[18:33]
	v_exp_f32_e32 v2, v2
	v_exp_f32_e32 v6, v6
	v_exp_f32_e32 v10, v10
	v_exp_f32_e32 v14, v14
	v_add_f32_e32 v122, 1.0, v4
	v_add_f32_e32 v123, 1.0, v8
	v_add_f32_e32 v118, 1.0, v12
	v_add_f32_e32 v119, 1.0, v16
	v_mfma_f32_32x32x16_bf16 v[18:33], v[114:117], v[166:169], v[18:33]
	v_exp_f32_e32 v3, v3
	v_fmac_f32_e32 v122, v2, v122
	v_exp_f32_e32 v2, v7
	v_fmac_f32_e32 v123, v6, v123
	v_exp_f32_e32 v6, v11
	v_exp_f32_e32 v7, v15
	v_fmac_f32_e32 v118, v10, v118
	v_fmac_f32_e32 v119, v14, v119
	v_mfma_f32_32x32x16_bf16 v[18:33], v[110:113], v[162:165], v[18:33]
	v_rcp_f32_e32 v10, v122
	v_rcp_f32_e32 v11, v123
	v_rcp_f32_e32 v14, v118
	v_rcp_f32_e32 v15, v119
	v_add_f32_e32 v3, 1.0, v3
	v_fmamk_f32 v4, v4, 0x4038aa3b, v183
	v_add_f32_e32 v2, 1.0, v2
	v_fmamk_f32 v8, v8, 0x4038aa3b, v183
	v_mfma_f32_32x32x16_bf16 v[18:33], v[106:109], v[158:161], v[18:33]
	v_rcp_f32_e32 v3, v3
	v_rcp_f32_e32 v2, v2
	v_add_f32_e32 v6, 1.0, v6
	v_fmamk_f32 v12, v12, 0x4038aa3b, v183
	v_exp_f32_e32 v110, v5
	v_add_f32_e32 v5, 1.0, v7
	v_exp_f32_e32 v111, v9
	v_fmac_f32_e32 v183, 0x4038aa3b, v16
	v_mfma_f32_32x32x16_bf16 v[18:33], v[102:105], v[154:157], v[18:33]
	v_mul_f32_e32 v106, v4, v10
	v_mul_f32_e32 v107, v8, v11
	v_rcp_f32_e32 v108, v6
	v_rcp_f32_e32 v109, v5
	v_exp_f32_e32 v112, v13
	v_exp_f32_e32 v113, v17
	v_mul_f32_e32 v102, v12, v14
	v_mul_f32_e32 v103, v183, v15
	v_mfma_f32_32x32x16_bf16 v[18:33], v[98:101], v[142:145], v[18:33]
	v_fmac_f32_e32 v106, v3, v205
	v_fmac_f32_e32 v107, v2, v204
	v_fmac_f32_e32 v102, v108, v203
	v_fmac_f32_e32 v103, v109, v202
	s_waitcnt lgkmcnt(3)
	v_mfma_f32_32x32x16_bf16 v[18:33], v[94:97], v[130:133], v[18:33]
	v_add_f32_e32 v98, 1.0, v110
	v_exp_f32_e32 v99, v106
	v_add_f32_e32 v100, 1.0, v111
	v_exp_f32_e32 v101, v107
	v_exp_f32_e32 v102, v102
	v_exp_f32_e32 v103, v103
	v_add_f32_e32 v94, 1.0, v112
	v_add_f32_e32 v95, 1.0, v113
	s_waitcnt lgkmcnt(2)
	v_mfma_f32_32x32x16_bf16 v[18:33], v[90:93], v[134:137], v[18:33]
	v_fmac_f32_e32 v98, v98, v99
	v_fmac_f32_e32 v100, v100, v101
	v_fmac_f32_e32 v94, v94, v102
	v_fmac_f32_e32 v95, v95, v103
	s_waitcnt lgkmcnt(1)
	v_mfma_f32_32x32x16_bf16 v[18:33], v[86:89], v[138:141], v[18:33]
	v_rcp_f32_e32 v90, v98
	v_rcp_f32_e32 v91, v100
	v_rcp_f32_e32 v92, v94
	v_rcp_f32_e32 v93, v95
	s_waitcnt lgkmcnt(0)
	v_mfma_f32_32x32x16_bf16 v[18:33], v[82:85], v[146:149], v[18:33]
	v_fma_f32 v86, -v99, v90, v90
	v_fma_f32 v87, -v101, v91, v91
	v_fma_f32 v88, -v102, v92, v92
	v_fma_f32 v89, -v103, v93, v93
	v_cvt_pk_bf16_f32 v254, v86, v87
	v_cvt_pk_bf16_f32 v255, v88, v89
	ds_write_b128 v211, v[252:255] offset:0
	s_waitcnt lgkmcnt(0)
	s_barrier
	v_mfma_f32_32x32x16_bf16 v[2:17], v[78:81], v[178:181], v[236:251]
	v_exp_f32_e32 v20, v20
	v_exp_f32_e32 v24, v24
	v_exp_f32_e32 v28, v28
	v_exp_f32_e32 v32, v32
	v_mfma_f32_32x32x16_bf16 v[2:17], v[74:77], v[174:177], v[2:17]
	v_exp_f32_e32 v18, v18
	v_add_f32_e32 v74, 1.0, v20
	v_exp_f32_e32 v22, v22
	v_add_f32_e32 v75, 1.0, v24
	v_exp_f32_e32 v26, v26
	v_exp_f32_e32 v30, v30
	v_mfma_f32_32x32x16_bf16 v[2:17], v[70:73], v[170:173], v[2:17]
	v_add_f32_e32 v70, 1.0, v28
	v_add_f32_e32 v71, 1.0, v32
	v_exp_f32_e32 v19, v19
	v_fmac_f32_e32 v74, v18, v74
	v_exp_f32_e32 v18, v23
	v_fmac_f32_e32 v75, v22, v75
	v_exp_f32_e32 v22, v27
	v_exp_f32_e32 v23, v31
	v_mfma_f32_32x32x16_bf16 v[2:17], v[66:69], v[166:169], v[2:17]
	v_fmac_f32_e32 v70, v26, v70
	v_fmac_f32_e32 v71, v30, v71
	v_mov_b32_e32 v27, 0xc038aa3b
	v_add_f32_e32 v19, 1.0, v19
	v_rcp_f32_e32 v26, v74
	v_rcp_f32_e32 v30, v75
	v_rcp_f32_e32 v31, v70
	v_rcp_f32_e32 v66, v71
	v_mfma_f32_32x32x16_bf16 v[2:17], v[62:65], v[162:165], v[2:17]
	v_fmamk_f32 v20, v20, 0x4038aa3b, v27
	v_add_f32_e32 v18, 1.0, v18
	v_fmamk_f32 v24, v24, 0x4038aa3b, v27
	v_add_f32_e32 v22, 1.0, v22
	v_fmamk_f32 v28, v28, 0x4038aa3b, v27
	v_rcp_f32_e32 v19, v19
	v_rcp_f32_e32 v18, v18
	v_exp_f32_e32 v21, v21
	v_exp_f32_e32 v25, v25
	v_mfma_f32_32x32x16_bf16 v[2:17], v[58:61], v[158:161], v[2:17]
	v_add_f32_e32 v23, 1.0, v23
	v_fmamk_f32 v32, v32, 0x4038aa3b, v27
	v_mul_f32_e32 v20, v20, v26
	v_mul_f32_e32 v24, v24, v30
	v_rcp_f32_e32 v22, v22
	v_rcp_f32_e32 v23, v23
	v_exp_f32_e32 v26, v29
	v_exp_f32_e32 v29, v33
	v_mfma_f32_32x32x16_bf16 v[2:17], v[54:57], v[154:157], v[2:17]
	v_mul_f32_e32 v28, v28, v31
	v_mul_f32_e32 v30, v32, v66
	v_fmac_f32_e32 v20, v19, v201
	v_fmac_f32_e32 v24, v18, v200
	v_fmac_f32_e32 v28, v22, v199
	v_fmac_f32_e32 v30, v23, v198
	v_mfma_f32_32x32x16_bf16 v[2:17], v[50:53], v[142:145], v[2:17]
	v_add_f32_e32 v18, 1.0, v21
	v_exp_f32_e32 v19, v20
	v_add_f32_e32 v20, 1.0, v25
	v_exp_f32_e32 v21, v24
	v_exp_f32_e32 v22, v28
	v_exp_f32_e32 v23, v30
	v_mfma_f32_32x32x16_bf16 v[2:17], v[46:49], v[130:133], v[2:17]
	v_add_f32_e32 v24, 1.0, v26
	v_add_f32_e32 v25, 1.0, v29
	v_fmac_f32_e32 v18, v18, v19
	v_fmac_f32_e32 v20, v20, v21
	v_fmac_f32_e32 v24, v24, v22
	v_fmac_f32_e32 v25, v25, v23
	v_mfma_f32_32x32x16_bf16 v[2:17], v[42:45], v[134:137], v[2:17]
	v_rcp_f32_e32 v18, v18
	v_rcp_f32_e32 v20, v20
	v_rcp_f32_e32 v24, v24
	v_rcp_f32_e32 v25, v25
	v_mfma_f32_32x32x16_bf16 v[2:17], v[38:41], v[138:141], v[2:17]
	v_fma_f32 v18, -v19, v18, v18
	v_fma_f32 v19, -v21, v20, v20
	v_fma_f32 v20, -v22, v24, v24
	v_fma_f32 v21, -v23, v25, v25
	v_mfma_f32_32x32x16_bf16 v[2:17], v[34:37], v[146:149], v[2:17]
	v_cvt_pk_bf16_f32 v252, v18, v19
	v_cvt_pk_bf16_f32 v253, v20, v21
	s_nop 9
	v_exp_f32_e32 v4, v4
	v_exp_f32_e32 v8, v8
	v_exp_f32_e32 v12, v12
	v_exp_f32_e32 v16, v16
	v_exp_f32_e32 v2, v2
	v_add_f32_e32 v18, 1.0, v4
	v_exp_f32_e32 v6, v6
	v_exp_f32_e32 v10, v10
	v_exp_f32_e32 v14, v14
	v_add_f32_e32 v19, 1.0, v8
	v_add_f32_e32 v20, 1.0, v12
	v_add_f32_e32 v21, 1.0, v16
	v_exp_f32_e32 v3, v3
	v_fmac_f32_e32 v18, v2, v18
	v_exp_f32_e32 v2, v7
	v_exp_f32_e32 v7, v11
	v_exp_f32_e32 v11, v15
	v_fmac_f32_e32 v19, v6, v19
	v_fmac_f32_e32 v20, v10, v20
	v_fmac_f32_e32 v21, v14, v21
	v_add_f32_e32 v3, 1.0, v3
	v_rcp_f32_e32 v6, v18
	v_rcp_f32_e32 v10, v19
	v_rcp_f32_e32 v14, v20
	v_rcp_f32_e32 v15, v21
	v_fmamk_f32 v4, v4, 0x4038aa3b, v27
	v_add_f32_e32 v2, 1.0, v2
	v_fmamk_f32 v8, v8, 0x4038aa3b, v27
	v_add_f32_e32 v7, 1.0, v7
	v_rcp_f32_e32 v3, v3
	v_rcp_f32_e32 v2, v2
	v_exp_f32_e32 v5, v5
	v_exp_f32_e32 v9, v9
	v_fmamk_f32 v12, v12, 0x4038aa3b, v27
	v_add_f32_e32 v11, 1.0, v11
	v_fmac_f32_e32 v27, 0x4038aa3b, v16
	v_mul_f32_e32 v4, v4, v6
	v_rcp_f32_e32 v6, v7
	v_rcp_f32_e32 v7, v11
	v_exp_f32_e32 v11, v13
	v_exp_f32_e32 v13, v17
	v_mul_f32_e32 v8, v8, v10
	v_mul_f32_e32 v10, v12, v14
	v_mul_f32_e32 v12, v27, v15
	v_fmac_f32_e32 v4, v3, v207
	v_fmac_f32_e32 v8, v2, v206
	v_fmac_f32_e32 v10, v6, v209
	v_fmac_f32_e32 v12, v7, v208
	v_add_f32_e32 v2, 1.0, v5
	v_exp_f32_e32 v3, v4
	v_exp_f32_e32 v4, v8
	v_exp_f32_e32 v5, v10
	v_exp_f32_e32 v6, v12
	v_add_f32_e32 v7, 1.0, v9
	v_add_f32_e32 v8, 1.0, v11
	v_add_f32_e32 v9, 1.0, v13
	v_fmac_f32_e32 v2, v2, v3
	v_fmac_f32_e32 v7, v7, v4
	v_fmac_f32_e32 v8, v8, v5
	v_fmac_f32_e32 v9, v9, v6
	v_rcp_f32_e32 v2, v2
	v_rcp_f32_e32 v7, v7
	v_rcp_f32_e32 v8, v8
	v_rcp_f32_e32 v9, v9
	v_fma_f32 v2, -v3, v2, v2
	v_fma_f32 v3, -v4, v7, v7
	v_fma_f32 v4, -v5, v8, v8
	v_fma_f32 v5, -v6, v9, v9
	v_cvt_pk_bf16_f32 v254, v2, v3
	v_cvt_pk_bf16_f32 v255, v4, v5
	ds_write_b128 v211, v[252:255] offset:8192
	s_waitcnt lgkmcnt(0)
	s_barrier
